# compiler-inserted full vmcnt(0) drains in front of six GEMM K-loops relaxed to the count that leaves the hand-pipelined operand loads (B(1) + A(1)) in flight
# speedup vs baseline: 1.0079x; 1.0079x over previous
.LBB0_947:
	s_or_b64 exec, exec, s[0:1]
	s_add_u32 s0, s70, 0x9038000
	s_addc_u32 s1, s71, 0
	s_ashr_i32 s22, s96, 2
	s_and_b32 s2, s22, 0xfffff8
	s_and_b32 s23, s96, 7
	s_bfe_u32 s8, s96, 0x20003
	s_or_b32 s2, s2, s23
	s_lshl_b32 s6, s8, 8
	s_lshl_b32 s4, s8, 9
	s_add_u32 s4, s70, s4
	s_addc_u32 s5, s71, 0
	s_add_u32 s24, s4, 0x20168000
	v_readfirstlane_b32 s4, v0
	s_addc_u32 s25, s5, 0
	s_lshr_b32 s10, s4, 6
	s_lshl_b32 s9, s2, 8
	s_lshl_b32 s2, s10, 1
	s_waitcnt vmcnt(23)
	v_lshlrev_b32_e32 v2, 4, v164
	v_or_b32_e32 v5, s2, v1
	s_and_b32 s5, s10, 4
	v_and_b32_e32 v146, 0x70, v2
	v_or_b32_e32 v2, s9, v147
	s_waitcnt vmcnt(7)
	v_and_or_b32 v6, v5, 3, s5
	s_lshr_b32 s5, s4, 1
	s_lshl_b32 s7, s10, 10
	s_barrier
	s_waitcnt vmcnt(4)
	v_lshl_or_b32 v18, v2, 11, v146
	s_and_b32 s16, s5, 0x7fffff80
	s_add_i32 s7, s7, 0
	s_mov_b32 s5, m0
	s_mov_b32 m0, s7
	s_nop 0
	global_load_lds_dwordx4 v18, s[0:1]
	s_mov_b32 m0, s5
	s_add_i32 s5, s7, 0x2000
	v_or_b32_e32 v2, 0x20000, v18
	s_mov_b32 s18, m0
	s_mov_b32 m0, s5
	s_nop 0
	global_load_lds_dwordx4 v2, s[0:1]
	s_mov_b32 m0, s18
	s_add_i32 s5, s7, 0x4000
	s_mov_b32 s3, 0
	v_or_b32_e32 v3, 0x40000, v18
	v_or_b32_e32 v4, 0x60000, v18
	s_bfe_u32 s17, s4, 0x20006
	s_mov_b32 s18, m0
	s_mov_b32 m0, s5
	s_nop 0
	global_load_lds_dwordx4 v3, s[0:1]
	s_mov_b32 m0, s18
	s_add_i32 s5, s7, 0x6000
	s_mov_b32 s18, m0
	s_mov_b32 m0, s5
	s_nop 0
	global_load_lds_dwordx4 v4, s[0:1]
	s_mov_b32 m0, s18
	s_lshl_b32 s11, s17, 7
	s_lshl_b64 s[18:19], s[2:3], 11
	s_add_u32 s18, s24, s18
	v_lshlrev_b32_e32 v6, 5, v6
	v_xor_b32_e32 v8, s11, v161
	v_lshlrev_b32_e32 v5, 9, v5
	s_addc_u32 s19, s25, s19
	v_lshl_or_b32 v163, v1, 11, v157
	v_or3_b32 v152, v162, v8, v160
	v_bitop3_b32 v8, s11, v161, 32 bitop3:0x36
	v_bitop3_b32 v157, v6, v5, v157 bitop3:0xde
	global_load_dwordx4 v[2:5], v163, s[18:19]
	s_add_i32 s18, s2, 16
	s_mov_b32 s19, s3
	v_or3_b32 v151, v162, v8, v160
	v_bitop3_b32 v8, s11, v161, 64 bitop3:0x36
	s_lshl_b64 s[18:19], s[18:19], 11
	v_or3_b32 v149, v162, v8, v160
	v_mov_b32_e32 v8, 0x60
	s_add_u32 s18, s24, s18
	v_or_b32_e32 v7, s16, v154
	v_bitop3_b32 v8, s11, v161, v8 bitop3:0x36
	s_addc_u32 s19, s25, s19
	v_or3_b32 v148, v162, v8, v160
	v_lshlrev_b32_e32 v34, 7, v7
	global_load_dwordx4 v[6:9], v163, s[18:19]
	s_add_i32 s18, s2, 32
	s_mov_b32 s19, s3
	s_lshl_b64 s[18:19], s[18:19], 11
	s_add_u32 s18, s24, s18
	s_addc_u32 s19, s25, s19
	global_load_dwordx4 v[10:13], v163, s[18:19]
	s_add_i32 s18, s2, 48
	s_mov_b32 s19, s3
	s_lshl_b64 s[18:19], s[18:19], 11
	s_add_u32 s18, s24, s18
	s_addc_u32 s19, s25, s19
	s_add_i32 s5, s7, 0x8000
	v_or_b32_e32 v19, 0x80, v18
	global_load_dwordx4 v[14:17], v163, s[18:19]
	s_mov_b32 s19, m0
	s_mov_b32 m0, s5
	s_nop 0
	global_load_lds_dwordx4 v19, s[0:1]
	s_mov_b32 m0, s19
	v_or_b32_e32 v19, 0x20080, v18
	s_add_i32 s5, s7, 0xa000
	s_mov_b32 s19, m0
	s_mov_b32 m0, s5
	s_nop 0
	global_load_lds_dwordx4 v19, s[0:1]
	s_mov_b32 m0, s19
	v_or_b32_e32 v19, 0x40080, v18
	s_add_i32 s5, s7, 0xc000
	v_or_b32_e32 v18, 0x60080, v18
	s_add_i32 s20, s2, 64
	s_mov_b32 s21, s3
	s_mov_b32 s19, m0
	s_mov_b32 m0, s5
	s_nop 0
	global_load_lds_dwordx4 v19, s[0:1]
	s_mov_b32 m0, s19
	s_add_i32 s5, s7, 0xe000
	s_mov_b32 s19, m0
	s_mov_b32 m0, s5
	s_nop 0
	global_load_lds_dwordx4 v18, s[0:1]
	s_mov_b32 m0, s19
	s_waitcnt vmcnt(2)
	s_waitcnt vmcnt(4)
	s_lshl_b64 s[20:21], s[20:21], 11
	v_add_u32_e32 v18, 0, v157
	s_add_u32 s20, s24, s20
	v_or_b32_e32 v150, v34, v159
	v_add_u32_e32 v159, 0x18000, v18
	s_addc_u32 s21, s25, s21
	ds_write_b128 v159, v[2:5]
	ds_write_b128 v159, v[6:9] offset:8192
	ds_write_b128 v159, v[10:13] offset:16384
	ds_write_b128 v159, v[14:17] offset:24576
	global_load_dwordx4 v[14:17], v163, s[20:21]
	s_add_i32 s20, s2, 0x50
	s_mov_b32 s21, s3
	s_lshl_b64 s[20:21], s[20:21], 11
	s_add_u32 s20, s24, s20
	s_addc_u32 s21, s25, s21
	global_load_dwordx4 v[10:13], v163, s[20:21]
	s_add_i32 s20, s2, 0x60
	s_mov_b32 s21, s3
	s_lshl_b64 s[20:21], s[20:21], 11
	s_add_u32 s20, s24, s20
	s_addc_u32 s21, s25, s21
	s_addk_i32 s2, 0x70
	global_load_dwordx4 v[6:9], v163, s[20:21]
	s_lshl_b64 s[20:21], s[2:3], 11
	s_add_u32 s20, s24, s20
	s_addc_u32 s21, s25, s21
	s_lshl_b64 s[4:5], s[4:5], 6
	s_and_b32 s5, s5, 63
	s_and_b32 s2, s4, 0xfffff000
	s_add_u32 s2, s24, s2
	s_addc_u32 s19, s25, s5
	s_lshl_b32 s4, s22, 19
	s_and_b32 s4, s4, 0xffc00000
	s_lshl_b32 s5, s23, 19
	global_load_dwordx4 v[2:5], v163, s[20:21]
	s_or_b32 s20, s4, s5
	v_lshlrev_b32_e32 v18, 11, v147
	s_waitcnt lgkmcnt(0)
	s_barrier
	v_or_b32_e32 v147, s20, v18
	v_or_b32_e32 v18, s4, v18
	v_or_b32_e32 v153, v34, v156
	v_or_b32_e32 v156, s5, v18
	v_mov_b32_e32 v18, 0
	s_mov_b32 s18, 0x8000
	s_mov_b32 s20, 0x10000
	s_mov_b64 s[4:5], 0
	v_mov_b32_e32 v19, v18
	v_mov_b32_e32 v20, v18
	v_mov_b32_e32 v21, v18
	v_mov_b32_e32 v30, v18
	v_mov_b32_e32 v31, v18
	v_mov_b32_e32 v32, v18
	v_mov_b32_e32 v33, v18
	v_mov_b32_e32 v22, v18
	v_mov_b32_e32 v23, v18
	v_mov_b32_e32 v24, v18
	v_mov_b32_e32 v25, v18
	v_mov_b32_e32 v26, v18
	v_mov_b32_e32 v27, v18
	v_mov_b32_e32 v28, v18
	v_mov_b32_e32 v29, v18
	v_mov_b32_e32 v34, v18
	v_mov_b32_e32 v35, v18
	v_mov_b32_e32 v36, v18
	v_mov_b32_e32 v37, v18
	s_waitcnt vmcnt(8)
	v_mov_b32_e32 v38, v18
	v_mov_b32_e32 v39, v18
	v_mov_b32_e32 v40, v18
	v_mov_b32_e32 v41, v18
	s_waitcnt vmcnt(8)
	v_mov_b32_e32 v42, v18
	v_mov_b32_e32 v43, v18
	v_mov_b32_e32 v44, v18
	v_mov_b32_e32 v45, v18
	v_mov_b32_e32 v50, v18
	v_mov_b32_e32 v51, v18
	v_mov_b32_e32 v52, v18
	v_mov_b32_e32 v53, v18
	v_mov_b32_e32 v66, v18
	v_mov_b32_e32 v67, v18
	v_mov_b32_e32 v68, v18
	v_mov_b32_e32 v69, v18
	v_mov_b32_e32 v78, v18
	v_mov_b32_e32 v79, v18
	v_mov_b32_e32 v80, v18
	v_mov_b32_e32 v81, v18
	v_mov_b32_e32 v90, v18
	v_mov_b32_e32 v91, v18
	v_mov_b32_e32 v92, v18
	v_mov_b32_e32 v93, v18
	v_mov_b32_e32 v94, v18
	v_mov_b32_e32 v95, v18
	v_mov_b32_e32 v96, v18
	v_mov_b32_e32 v97, v18
	v_mov_b32_e32 v118, v18
	v_mov_b32_e32 v119, v18
	v_mov_b32_e32 v120, v18
	v_mov_b32_e32 v121, v18
	v_mov_b32_e32 v126, v18
	v_mov_b32_e32 v127, v18
	v_mov_b32_e32 v128, v18
	v_mov_b32_e32 v129, v18
	v_mov_b32_e32 v138, v18
	v_mov_b32_e32 v139, v18
	v_mov_b32_e32 v140, v18
	v_mov_b32_e32 v141, v18
	v_mov_b32_e32 v142, v18
	v_mov_b32_e32 v143, v18
	v_mov_b32_e32 v144, v18
	v_mov_b32_e32 v145, v18
	v_mov_b32_e32 v114, v18
	v_mov_b32_e32 v115, v18
	v_mov_b32_e32 v116, v18
	v_mov_b32_e32 v117, v18
	v_mov_b32_e32 v122, v18
	v_mov_b32_e32 v123, v18
	v_mov_b32_e32 v124, v18
	v_mov_b32_e32 v125, v18
	v_mov_b32_e32 v134, v18
	v_mov_b32_e32 v135, v18
	v_mov_b32_e32 v136, v18
	v_mov_b32_e32 v137, v18
	v_mov_b32_e32 v130, v18
	v_mov_b32_e32 v131, v18
	v_mov_b32_e32 v132, v18
	v_mov_b32_e32 v133, v18
	v_mov_b32_e32 v98, v18
	v_mov_b32_e32 v99, v18
	v_mov_b32_e32 v100, v18
	v_mov_b32_e32 v101, v18
	v_mov_b32_e32 v102, v18
	v_mov_b32_e32 v103, v18
	v_mov_b32_e32 v104, v18
	v_mov_b32_e32 v105, v18
	v_mov_b32_e32 v110, v18
	v_mov_b32_e32 v111, v18
	v_mov_b32_e32 v112, v18
	v_mov_b32_e32 v113, v18
	v_mov_b32_e32 v106, v18
	v_mov_b32_e32 v107, v18
	v_mov_b32_e32 v108, v18
	v_mov_b32_e32 v109, v18
	v_mov_b32_e32 v70, v18
	v_mov_b32_e32 v71, v18
	v_mov_b32_e32 v72, v18
	v_mov_b32_e32 v73, v18
	v_mov_b32_e32 v82, v18
	v_mov_b32_e32 v83, v18
	v_mov_b32_e32 v84, v18
	v_mov_b32_e32 v85, v18
	v_mov_b32_e32 v86, v18
	v_mov_b32_e32 v87, v18
	v_mov_b32_e32 v88, v18
	v_mov_b32_e32 v89, v18
	v_mov_b32_e32 v74, v18
	v_mov_b32_e32 v75, v18
	v_mov_b32_e32 v76, v18
	v_mov_b32_e32 v77, v18
	v_mov_b32_e32 v46, v18
	v_mov_b32_e32 v47, v18
	v_mov_b32_e32 v48, v18
	v_mov_b32_e32 v49, v18
	v_mov_b32_e32 v58, v18
	v_mov_b32_e32 v59, v18
	v_mov_b32_e32 v60, v18
	v_mov_b32_e32 v61, v18
	v_mov_b32_e32 v62, v18
	v_mov_b32_e32 v63, v18
	v_mov_b32_e32 v64, v18
	v_mov_b32_e32 v65, v18
	v_mov_b32_e32 v54, v18
	v_mov_b32_e32 v55, v18
	v_mov_b32_e32 v56, v18
	v_mov_b32_e32 v57, v18

.LBB0_1038:
	s_ashr_i32 s30, s0, 2
	s_and_b32 s1, s30, 0xfffff8
	s_and_b32 s31, s0, 7
	s_bfe_u32 s20, s0, 0x20003
	s_or_b32 s1, s1, s31
	s_lshl_b32 s22, s20, 8
	s_lshl_b32 s0, s20, 9
	s_add_u32 s33, s16, s0
	s_addc_u32 s34, s17, 0
	s_lshl_b32 s21, s1, 8
	v_readfirstlane_b32 s0, v0
	s_lshr_b32 s23, s0, 6
	v_or_b32_e32 v2, s21, v159
	v_lshlrev_b32_e32 v2, 11, v2
	v_or_b32_e32 v3, 0x20000, v171
	s_lshl_b32 s2, s23, 1
	s_waitcnt vmcnt(4)
	v_or_b32_e32 v18, v2, v171
	v_add_u32_e32 v19, v2, v3
	v_add_u32_e32 v20, v2, v210
	s_bfe_u32 s26, s0, 0x20006
	v_or_b32_e32 v2, s2, v253
	s_and_b32 s1, s23, 4
	v_and_or_b32 v4, v2, 3, s1
	s_lshr_b32 s1, s0, 1
	s_lshl_b32 s24, s26, 7
	s_and_b32 s25, s1, 0x7fffff80
	s_or_b32 s1, s24, 32
	v_bitop3_b32 v151, s1, v212, v207 bitop3:0xde
	s_or_b32 s1, s24, 64
	v_bitop3_b32 v149, s1, v212, v207 bitop3:0xde
	s_or_b32 s1, s24, 0x60
	s_lshl_b32 s27, s23, 10
	v_bitop3_b32 v148, s1, v212, v207 bitop3:0xde
	s_add_i32 s27, s27, 0
	s_mov_b32 s1, m0
	s_mov_b32 m0, s27
	s_nop 0
	global_load_lds_dwordx4 v18, s[6:7]
	s_mov_b32 m0, s1
	s_add_i32 s1, s27, 0x2000
	s_mov_b32 s28, m0
	s_mov_b32 m0, s1
	s_nop 0
	global_load_lds_dwordx4 v19, s[6:7]
	s_mov_b32 m0, s28
	s_add_i32 s1, s27, 0x4000
	v_or_b32_e32 v3, 0x40000, v18
	s_mov_b32 s28, m0
	s_mov_b32 m0, s1
	s_nop 0
	global_load_lds_dwordx4 v3, s[6:7]
	s_mov_b32 m0, s28
	s_add_i32 s1, s27, 0x6000
	s_mov_b32 s28, m0
	s_mov_b32 m0, s1
	s_nop 0
	global_load_lds_dwordx4 v20, s[6:7]
	s_mov_b32 m0, s28
	s_lshl_b64 s[28:29], s[2:3], 11
	s_add_u32 s28, s33, s28
	v_lshlrev_b32_e32 v4, 5, v4
	s_waitcnt lgkmcnt(0)
	v_or_b32_e32 v5, s25, v1
	v_lshlrev_b32_e32 v2, 9, v2
	s_addc_u32 s29, s34, s29
	v_lshlrev_b32_e32 v34, 7, v5
	v_bitop3_b32 v154, v4, v2, v254 bitop3:0xde
	global_load_dwordx4 v[2:5], v208, s[28:29]
	s_add_i32 s28, s2, 16
	s_mov_b32 s29, s3
	s_lshl_b64 s[28:29], s[28:29], 11
	s_add_u32 s28, s33, s28
	s_addc_u32 s29, s34, s29
	global_load_dwordx4 v[6:9], v208, s[28:29]
	s_add_i32 s28, s2, 32
	s_mov_b32 s29, s3
	s_lshl_b64 s[28:29], s[28:29], 11
	s_add_u32 s28, s33, s28
	s_addc_u32 s29, s34, s29
	global_load_dwordx4 v[10:13], v208, s[28:29]
	s_add_i32 s28, s2, 48
	s_mov_b32 s29, s3
	s_lshl_b64 s[28:29], s[28:29], 11
	s_add_u32 s28, s33, s28
	s_addc_u32 s29, s34, s29
	s_add_i32 s1, s27, 0x8000
	global_load_dwordx4 v[14:17], v208, s[28:29]
	v_or_b32_e32 v21, 0x80, v18
	s_mov_b32 s28, m0
	s_mov_b32 m0, s1
	s_nop 0
	global_load_lds_dwordx4 v21, s[6:7]
	s_mov_b32 m0, s28
	s_add_i32 s1, s27, 0xa000
	v_or_b32_e32 v19, 0x80, v19
	s_mov_b32 s28, m0
	s_mov_b32 m0, s1
	s_nop 0
	global_load_lds_dwordx4 v19, s[6:7]
	s_mov_b32 m0, s28
	v_or_b32_e32 v18, 0x40080, v18
	s_add_i32 s1, s27, 0xc000
	s_mov_b32 s28, m0
	s_mov_b32 m0, s1
	s_nop 0
	global_load_lds_dwordx4 v18, s[6:7]
	s_mov_b32 m0, s28
	v_or_b32_e32 v18, 0x80, v20
	s_add_i32 s1, s27, 0xe000
	s_mov_b32 s28, m0
	s_mov_b32 m0, s1
	s_nop 0
	global_load_lds_dwordx4 v18, s[6:7]
	s_mov_b32 m0, s28
	s_add_i32 s28, s2, 64
	s_mov_b32 s29, s3
	s_waitcnt vmcnt(2)
	s_waitcnt vmcnt(4)
	s_lshl_b64 s[28:29], s[28:29], 11
	v_add_u32_e32 v18, 0, v154
	s_add_u32 s28, s33, s28
	v_add_u32_e32 v155, 0x18000, v18
	s_addc_u32 s29, s34, s29
	ds_write_b128 v155, v[2:5]
	ds_write_b128 v155, v[6:9] offset:8192
	ds_write_b128 v155, v[10:13] offset:16384
	ds_write_b128 v155, v[14:17] offset:24576
	global_load_dwordx4 v[14:17], v208, s[28:29]
	s_add_i32 s28, s2, 0x50
	s_mov_b32 s29, s3
	s_lshl_b64 s[28:29], s[28:29], 11
	s_add_u32 s28, s33, s28
	s_addc_u32 s29, s34, s29
	global_load_dwordx4 v[10:13], v208, s[28:29]
	s_add_i32 s28, s2, 0x60
	s_mov_b32 s29, s3
	s_lshl_b64 s[28:29], s[28:29], 11
	s_add_u32 s28, s33, s28
	s_addc_u32 s29, s34, s29
	s_addk_i32 s2, 0x70
	global_load_dwordx4 v[6:9], v208, s[28:29]
	s_lshl_b64 s[28:29], s[2:3], 11
	s_add_u32 s28, s33, s28
	s_addc_u32 s29, s34, s29
	s_lshl_b64 s[0:1], s[0:1], 6
	s_and_b32 s1, s1, 63
	s_and_b32 s0, s0, 0xfffff000
	s_add_u32 s2, s33, s0
	global_load_dwordx4 v[2:5], v208, s[28:29]
	s_addc_u32 s28, s34, s1
	s_lshl_b32 s0, s30, 19
	s_and_b32 s0, s0, 0xffc00000
	s_waitcnt lgkmcnt(0)
	s_barrier
	v_lshl_or_b32 v18, v159, 11, s0
	v_lshl_or_b32 v18, s31, 19, v18
	v_bitop3_b32 v152, s24, v212, v207 bitop3:0xde
	v_or_b32_e32 v150, v34, v209
	v_or_b32_e32 v153, v34, v206
	v_add_u32_e32 v156, v213, v18
	s_mov_b64 s[0:1], 0
	s_mov_b32 s29, 0x8000
	s_mov_b32 s30, 0
	s_mov_b32 s31, 0x10000
	v_mov_b32_e32 v18, v147
	v_mov_b32_e32 v19, v147
	v_mov_b32_e32 v20, v147
	v_mov_b32_e32 v21, v147
	v_mov_b32_e32 v22, v147
	v_mov_b32_e32 v23, v147
	v_mov_b32_e32 v24, v147
	v_mov_b32_e32 v25, v147
	v_mov_b32_e32 v26, v147
	v_mov_b32_e32 v27, v147
	v_mov_b32_e32 v28, v147
	v_mov_b32_e32 v29, v147
	v_mov_b32_e32 v30, v147
	v_mov_b32_e32 v31, v147
	v_mov_b32_e32 v32, v147
	v_mov_b32_e32 v33, v147
	v_mov_b32_e32 v34, v147
	v_mov_b32_e32 v35, v147
	v_mov_b32_e32 v36, v147
	v_mov_b32_e32 v37, v147
	s_waitcnt vmcnt(8)
	v_mov_b32_e32 v38, v147
	v_mov_b32_e32 v39, v147
	v_mov_b32_e32 v40, v147
	v_mov_b32_e32 v41, v147
	s_waitcnt vmcnt(8)
	v_mov_b32_e32 v42, v147
	v_mov_b32_e32 v43, v147
	v_mov_b32_e32 v44, v147
	v_mov_b32_e32 v45, v147
	v_mov_b32_e32 v54, v147
	v_mov_b32_e32 v55, v147
	v_mov_b32_e32 v56, v147
	v_mov_b32_e32 v57, v147
	v_mov_b32_e32 v66, v147
	v_mov_b32_e32 v67, v147
	v_mov_b32_e32 v68, v147
	v_mov_b32_e32 v69, v147
	v_mov_b32_e32 v78, v147
	v_mov_b32_e32 v79, v147
	v_mov_b32_e32 v80, v147
	v_mov_b32_e32 v81, v147
	v_mov_b32_e32 v90, v147
	v_mov_b32_e32 v91, v147
	v_mov_b32_e32 v92, v147
	v_mov_b32_e32 v93, v147
	v_mov_b32_e32 v94, v147
	v_mov_b32_e32 v95, v147
	v_mov_b32_e32 v96, v147
	v_mov_b32_e32 v97, v147
	v_mov_b32_e32 v114, v147
	v_mov_b32_e32 v115, v147
	v_mov_b32_e32 v116, v147
	v_mov_b32_e32 v117, v147
	v_mov_b32_e32 v122, v147
	v_mov_b32_e32 v123, v147
	v_mov_b32_e32 v124, v147
	v_mov_b32_e32 v125, v147
	v_mov_b32_e32 v138, v147
	v_mov_b32_e32 v139, v147
	v_mov_b32_e32 v140, v147
	v_mov_b32_e32 v141, v147
	v_mov_b32_e32 v142, v147
	v_mov_b32_e32 v143, v147
	v_mov_b32_e32 v144, v147
	v_mov_b32_e32 v145, v147
	v_mov_b32_e32 v118, v147
	v_mov_b32_e32 v119, v147
	v_mov_b32_e32 v120, v147
	v_mov_b32_e32 v121, v147
	v_mov_b32_e32 v126, v147
	v_mov_b32_e32 v127, v147
	v_mov_b32_e32 v128, v147
	v_mov_b32_e32 v129, v147
	v_mov_b32_e32 v134, v147
	v_mov_b32_e32 v135, v147
	v_mov_b32_e32 v136, v147
	v_mov_b32_e32 v137, v147
	v_mov_b32_e32 v130, v147
	v_mov_b32_e32 v131, v147
	v_mov_b32_e32 v132, v147
	v_mov_b32_e32 v133, v147
	v_mov_b32_e32 v98, v147
	v_mov_b32_e32 v99, v147
	v_mov_b32_e32 v100, v147
	v_mov_b32_e32 v101, v147
	v_mov_b32_e32 v102, v147
	v_mov_b32_e32 v103, v147
	v_mov_b32_e32 v104, v147
	v_mov_b32_e32 v105, v147
	v_mov_b32_e32 v110, v147
	v_mov_b32_e32 v111, v147
	v_mov_b32_e32 v112, v147
	v_mov_b32_e32 v113, v147
	v_mov_b32_e32 v106, v147
	v_mov_b32_e32 v107, v147
	v_mov_b32_e32 v108, v147
	v_mov_b32_e32 v109, v147
	v_mov_b32_e32 v70, v147
	v_mov_b32_e32 v71, v147
	v_mov_b32_e32 v72, v147
	v_mov_b32_e32 v73, v147
	v_mov_b32_e32 v82, v147
	v_mov_b32_e32 v83, v147
	v_mov_b32_e32 v84, v147
	v_mov_b32_e32 v85, v147
	v_mov_b32_e32 v86, v147
	v_mov_b32_e32 v87, v147
	v_mov_b32_e32 v88, v147
	v_mov_b32_e32 v89, v147
	v_mov_b32_e32 v74, v147
	v_mov_b32_e32 v75, v147
	v_mov_b32_e32 v76, v147
	v_mov_b32_e32 v77, v147
	v_mov_b32_e32 v46, v147
	v_mov_b32_e32 v47, v147
	v_mov_b32_e32 v48, v147
	v_mov_b32_e32 v49, v147
	v_mov_b32_e32 v58, v147
	v_mov_b32_e32 v59, v147
	v_mov_b32_e32 v60, v147
	v_mov_b32_e32 v61, v147
	v_mov_b32_e32 v62, v147
	v_mov_b32_e32 v63, v147
	v_mov_b32_e32 v64, v147
	v_mov_b32_e32 v65, v147
	v_mov_b32_e32 v50, v147
	v_mov_b32_e32 v51, v147
	v_mov_b32_e32 v52, v147
	v_mov_b32_e32 v53, v147

.LBB0_1432:
	s_lshr_b32 s33, s2, 6
	s_lshl_b32 s3, s33, 1
	v_or_b32_e32 v2, s3, v193
	s_and_b32 s36, s33, 4
	s_and_b32 s37, s2, 0xc0
	v_and_or_b32 v3, v2, 3, s36
	s_lshr_b32 s36, s2, 1
	s_or_b32 s2, s37, 32
	v_bitop3_b32 v183, s2, v203, v198 bitop3:0xde
	s_or_b32 s2, s37, 0x100
	v_bitop3_b32 v181, s2, v203, v198 bitop3:0xde
	s_or_b32 s2, s37, 0x120
	s_lshl_b32 s38, s33, 10
	v_bitop3_b32 v172, s2, v203, v198 bitop3:0xde
	s_add_i32 s38, s38, 0
	s_mov_b32 s2, m0
	s_mov_b32 m0, s38
	s_nop 0
	global_load_lds_dwordx4 v34, s[18:19]
	s_mov_b32 m0, s2
	s_add_i32 s2, s38, 0x2000
	s_mov_b32 s39, m0
	s_mov_b32 m0, s2
	s_nop 0
	global_load_lds_dwordx4 v35, s[18:19]
	s_mov_b32 m0, s39
	s_add_i32 s2, s38, 0x4000
	s_mov_b32 s39, m0
	s_mov_b32 m0, s2
	s_nop 0
	global_load_lds_dwordx4 v36, s[18:19]
	s_mov_b32 m0, s39
	s_add_i32 s2, s38, 0x6000
	v_lshlrev_b32_e32 v2, 9, v2
	v_lshlrev_b32_e32 v3, 5, v3
	s_and_b32 s36, s36, 0x7fffff80
	s_mov_b32 s39, m0
	s_mov_b32 m0, s2
	s_nop 0
	global_load_lds_dwordx4 v37, s[18:19]
	s_mov_b32 m0, s39
	s_mul_i32 s2, s33, 0x5800
	v_bitop3_b32 v214, v3, v2, v194 bitop3:0xde
	v_or_b32_e32 v2, s36, v1
	s_mul_hi_u32 s39, s3, 0x2c00
	s_add_u32 s40, s59, s2
	s_waitcnt vmcnt(1)
	v_lshlrev_b32_e32 v38, 7, v2
	s_addc_u32 s41, s73, s39
	global_load_dwordx4 v[2:5], v199, s[40:41]
	s_add_i32 s40, s3, 16
	s_add_i32 s83, s2, 0x2c000
	s_mul_hi_u32 s84, s40, 0x2c00
	s_add_u32 s40, s59, s83
	s_addc_u32 s41, s73, s84
	global_load_dwordx4 v[6:9], v199, s[40:41]
	s_add_i32 s40, s3, 32
	s_add_i32 s85, s2, 0x58000
	s_mul_hi_u32 s86, s40, 0x2c00
	s_add_u32 s40, s59, s85
	s_addc_u32 s41, s73, s86
	global_load_dwordx4 v[10:13], v199, s[40:41]
	s_add_i32 s40, s3, 48
	s_add_i32 s87, s2, 0x84000
	s_mul_hi_u32 s88, s40, 0x2c00
	s_add_u32 s40, s59, s87
	s_addc_u32 s41, s73, s88
	global_load_dwordx4 v[14:17], v199, s[40:41]
	s_add_u32 s40, s74, s2
	s_addc_u32 s41, s75, s39
	global_load_dwordx4 v[18:21], v199, s[40:41]
	s_add_u32 s40, s74, s83
	s_addc_u32 s41, s75, s84
	global_load_dwordx4 v[22:25], v199, s[40:41]
	s_add_u32 s40, s74, s85
	s_addc_u32 s41, s75, s86
	global_load_dwordx4 v[26:29], v199, s[40:41]
	s_add_u32 s40, s74, s87
	s_addc_u32 s41, s75, s88
	global_load_dwordx4 v[30:33], v199, s[40:41]
	s_add_i32 s40, s38, 0x8000
	v_add_u32_e32 v39, 0x80, v34
	s_mov_b32 s41, m0
	s_mov_b32 m0, s40
	s_nop 0
	global_load_lds_dwordx4 v39, s[18:19]
	s_mov_b32 m0, s41
	v_add_u32_e32 v39, 0x80, v35
	s_add_i32 s40, s38, 0xa000
	s_mov_b32 s41, m0
	s_mov_b32 m0, s40
	s_nop 0
	global_load_lds_dwordx4 v39, s[18:19]
	s_mov_b32 m0, s41
	v_add_u32_e32 v39, 0x80, v36
	s_add_i32 s40, s38, 0xc000
	s_mov_b32 s41, m0
	s_mov_b32 m0, s40
	s_nop 0
	global_load_lds_dwordx4 v39, s[18:19]
	s_mov_b32 m0, s41
	v_add_u32_e32 v39, 0x80, v37
	s_add_i32 s40, s38, 0xe000
	s_mov_b32 s41, m0
	s_mov_b32 m0, s40
	s_nop 0
	global_load_lds_dwordx4 v39, s[18:19]
	s_mov_b32 m0, s41
	s_waitcnt vmcnt(4)
	v_add_u32_e32 v217, s52, v214
	v_cvt_pk_bf16_f32 v2, v2, v3
	v_cvt_pk_bf16_f32 v3, v4, v5
	v_cvt_pk_bf16_f32 v4, v6, v7
	v_cvt_pk_bf16_f32 v5, v8, v9
	v_or_b32_e32 v213, 0x100, v214
	ds_write2st64_b64 v217, v[2:3], v[4:5] offset1:16
	v_cvt_pk_bf16_f32 v2, v10, v11
	v_cvt_pk_bf16_f32 v3, v12, v13
	v_cvt_pk_bf16_f32 v4, v14, v15
	v_cvt_pk_bf16_f32 v5, v16, v17
	ds_write2st64_b64 v217, v[2:3], v[4:5] offset0:32 offset1:48
	v_cvt_pk_bf16_f32 v2, v18, v19
	v_cvt_pk_bf16_f32 v3, v20, v21
	v_add_u32_e32 v6, s52, v213
	v_cvt_pk_bf16_f32 v4, v22, v23
	v_cvt_pk_bf16_f32 v5, v24, v25
	s_add_i32 s40, s3, 64
	s_add_i32 s83, s2, 0xb0000
	ds_write2st64_b64 v6, v[2:3], v[4:5] offset1:16
	v_cvt_pk_bf16_f32 v2, v26, v27
	v_cvt_pk_bf16_f32 v3, v28, v29
	v_cvt_pk_bf16_f32 v4, v30, v31
	v_cvt_pk_bf16_f32 v5, v32, v33
	s_mul_hi_u32 s84, s40, 0x2c00
	s_add_u32 s40, s59, s83
	ds_write2st64_b64 v6, v[2:3], v[4:5] offset0:32 offset1:48
	s_addc_u32 s41, s73, s84
	global_load_dwordx4 v[30:33], v199, s[40:41]
	s_add_i32 s40, s3, 0x50
	s_add_i32 s85, s2, 0xdc000
	s_mul_hi_u32 s86, s40, 0x2c00
	s_add_u32 s40, s59, s85
	s_addc_u32 s41, s73, s86
	global_load_dwordx4 v[26:29], v199, s[40:41]
	s_add_i32 s40, s3, 0x60
	s_add_i32 s87, s2, 0x108000
	s_mul_hi_u32 s88, s40, 0x2c00
	s_add_u32 s40, s59, s87
	s_addc_u32 s41, s73, s88
	s_addk_i32 s3, 0x70
	s_add_i32 s89, s2, 0x134000
	global_load_dwordx4 v[22:25], v199, s[40:41]
	s_mul_hi_u32 s3, s3, 0x2c00
	s_add_u32 s40, s59, s89
	s_addc_u32 s41, s73, s3
	global_load_dwordx4 v[18:21], v199, s[40:41]
	s_add_u32 s40, s74, s83
	s_addc_u32 s41, s75, s84
	global_load_dwordx4 v[14:17], v199, s[40:41]
	s_add_u32 s40, s74, s85
	s_addc_u32 s41, s75, s86
	global_load_dwordx4 v[10:13], v199, s[40:41]
	s_add_u32 s40, s74, s87
	s_addc_u32 s41, s75, s88
	global_load_dwordx4 v[6:9], v199, s[40:41]
	s_add_u32 s40, s74, s89
	s_addc_u32 s41, s75, s3
	global_load_dwordx4 v[2:5], v199, s[40:41]
	s_mul_hi_u32 s3, s33, 0x5800
	s_add_u32 s40, s74, s2
	s_waitcnt lgkmcnt(0)
	s_barrier
	s_addc_u32 s41, s75, s3
	s_add_u32 s83, s59, s2
	v_add_u32_e32 v221, 0x100, v34
	v_mov_b32_e32 v34, 0
	v_bitop3_b32 v212, s37, v203, v198 bitop3:0xde
	v_or_b32_e32 v215, v38, v196
	s_mov_b32 s39, 0x8000
	v_or_b32_e32 v216, v38, v197
	s_addc_u32 s84, s73, s3
	v_add_u32_e32 v218, 0x100, v37
	v_add_u32_e32 v219, 0x100, v36
	v_add_u32_e32 v220, 0x100, v35
	s_mov_b32 s85, 0x10000
	s_mov_b32 s86, 0
	s_mov_b64 s[2:3], 0
	v_mov_b32_e32 v35, v34
	v_mov_b32_e32 v36, v34
	v_mov_b32_e32 v37, v34
	v_mov_b32_e32 v38, v34
	v_mov_b32_e32 v39, v34
	v_mov_b32_e32 v40, v34
	v_mov_b32_e32 v41, v34
	v_mov_b32_e32 v46, v34
	v_mov_b32_e32 v47, v34
	v_mov_b32_e32 v48, v34
	v_mov_b32_e32 v49, v34
	v_mov_b32_e32 v50, v34
	v_mov_b32_e32 v51, v34
	v_mov_b32_e32 v52, v34
	v_mov_b32_e32 v53, v34
	s_waitcnt vmcnt(12)
	v_mov_b32_e32 v42, v34
	v_mov_b32_e32 v43, v34
	v_mov_b32_e32 v44, v34
	v_mov_b32_e32 v45, v34
	v_mov_b32_e32 v54, v34
	v_mov_b32_e32 v55, v34
	v_mov_b32_e32 v56, v34
	v_mov_b32_e32 v57, v34
	v_mov_b32_e32 v58, v34
	v_mov_b32_e32 v59, v34
	v_mov_b32_e32 v60, v34
	v_mov_b32_e32 v61, v34
	v_mov_b32_e32 v62, v34
	v_mov_b32_e32 v63, v34
	v_mov_b32_e32 v64, v34
	v_mov_b32_e32 v65, v34
	v_mov_b32_e32 v66, v34
	v_mov_b32_e32 v67, v34
	v_mov_b32_e32 v68, v34
	v_mov_b32_e32 v69, v34
	v_mov_b32_e32 v70, v34
	v_mov_b32_e32 v71, v34
	v_mov_b32_e32 v72, v34
	v_mov_b32_e32 v73, v34
	v_mov_b32_e32 v74, v34
	v_mov_b32_e32 v75, v34
	v_mov_b32_e32 v76, v34
	v_mov_b32_e32 v77, v34
	v_mov_b32_e32 v78, v34
	v_mov_b32_e32 v79, v34
	v_mov_b32_e32 v80, v34
	v_mov_b32_e32 v81, v34
	v_mov_b32_e32 v82, v34
	v_mov_b32_e32 v83, v34
	v_mov_b32_e32 v84, v34
	v_mov_b32_e32 v85, v34
	v_mov_b32_e32 v86, v34
	v_mov_b32_e32 v87, v34
	v_mov_b32_e32 v88, v34
	v_mov_b32_e32 v89, v34
	v_mov_b32_e32 v90, v34
	v_mov_b32_e32 v91, v34
	v_mov_b32_e32 v92, v34
	v_mov_b32_e32 v93, v34
	v_mov_b32_e32 v94, v34
	v_mov_b32_e32 v95, v34
	v_mov_b32_e32 v96, v34
	v_mov_b32_e32 v97, v34
	v_mov_b32_e32 v98, v34
	v_mov_b32_e32 v99, v34
	v_mov_b32_e32 v100, v34
	v_mov_b32_e32 v101, v34
	v_mov_b32_e32 v102, v34
	v_mov_b32_e32 v103, v34
	v_mov_b32_e32 v104, v34
	v_mov_b32_e32 v105, v34
	v_mov_b32_e32 v106, v34
	v_mov_b32_e32 v107, v34
	v_mov_b32_e32 v108, v34
	v_mov_b32_e32 v109, v34
	v_mov_b32_e32 v110, v34
	v_mov_b32_e32 v111, v34
	v_mov_b32_e32 v112, v34
	v_mov_b32_e32 v113, v34
	v_mov_b32_e32 v114, v34
	v_mov_b32_e32 v115, v34
	v_mov_b32_e32 v116, v34
	v_mov_b32_e32 v117, v34
	v_mov_b32_e32 v118, v34
	v_mov_b32_e32 v119, v34
	v_mov_b32_e32 v120, v34
	v_mov_b32_e32 v121, v34
	v_mov_b32_e32 v122, v34
	v_mov_b32_e32 v123, v34
	v_mov_b32_e32 v124, v34
	v_mov_b32_e32 v125, v34
	v_mov_b32_e32 v126, v34
	v_mov_b32_e32 v127, v34
	v_mov_b32_e32 v128, v34
	v_mov_b32_e32 v129, v34
	v_mov_b32_e32 v130, v34
	v_mov_b32_e32 v131, v34
	v_mov_b32_e32 v132, v34
	v_mov_b32_e32 v133, v34
	v_mov_b32_e32 v134, v34
	v_mov_b32_e32 v135, v34
	v_mov_b32_e32 v136, v34
	v_mov_b32_e32 v137, v34
	v_mov_b32_e32 v138, v34
	v_mov_b32_e32 v139, v34
	v_mov_b32_e32 v140, v34
	v_mov_b32_e32 v141, v34
	v_mov_b32_e32 v142, v34
	v_mov_b32_e32 v143, v34
	v_mov_b32_e32 v144, v34
	v_mov_b32_e32 v145, v34
	v_mov_b32_e32 v146, v34
	v_mov_b32_e32 v147, v34
	v_mov_b32_e32 v148, v34
	v_mov_b32_e32 v149, v34
	v_mov_b32_e32 v150, v34
	v_mov_b32_e32 v151, v34
	v_mov_b32_e32 v152, v34
	v_mov_b32_e32 v153, v34
	v_mov_b32_e32 v154, v34
	v_mov_b32_e32 v155, v34
	v_mov_b32_e32 v156, v34
	v_mov_b32_e32 v157, v34
	v_mov_b32_e32 v158, v34
	v_mov_b32_e32 v159, v34
	v_mov_b32_e32 v160, v34
	v_mov_b32_e32 v161, v34

.LBB0_1445:
	s_lshr_b32 s2, s3, 6
	s_bfe_u32 s33, s3, 0x20006
	s_lshl_b32 s40, s2, 1
	s_lshr_b32 s3, s3, 1
	v_or_b32_e32 v2, s40, v193
	s_and_b32 s36, s2, 4
	s_and_b32 s83, s3, 0x7fffff80
	s_lshl_b32 s3, s33, 6
	v_and_or_b32 v3, v2, 3, s36
	s_or_b32 s36, s3, 32
	v_bitop3_b32 v184, s36, v203, v198 bitop3:0xde
	s_or_b32 s36, s3, 0x100
	v_bitop3_b32 v185, s3, v203, v198 bitop3:0xde
	v_bitop3_b32 v181, s36, v203, v198 bitop3:0xde
	s_or_b32 s3, s3, 0x120
	s_lshl_b32 s36, s2, 10
	v_bitop3_b32 v172, s3, v203, v198 bitop3:0xde
	s_add_i32 s36, s36, 0
	s_mov_b32 s3, m0
	s_mov_b32 m0, s36
	s_nop 0
	global_load_lds_dwordx4 v34, s[18:19]
	s_mov_b32 m0, s3
	s_add_i32 s3, s36, 0x2000
	s_mov_b32 s37, m0
	s_mov_b32 m0, s3
	s_nop 0
	global_load_lds_dwordx4 v35, s[18:19]
	s_mov_b32 m0, s37
	s_add_i32 s3, s36, 0x4000
	s_mov_b32 s37, m0
	s_mov_b32 m0, s3
	s_nop 0
	global_load_lds_dwordx4 v36, s[18:19]
	s_mov_b32 m0, s37
	s_add_i32 s3, s36, 0x6000
	v_lshlrev_b32_e32 v2, 9, v2
	v_lshlrev_b32_e32 v3, 5, v3
	s_mov_b32 s37, m0
	s_mov_b32 m0, s3
	s_nop 0
	global_load_lds_dwordx4 v37, s[18:19]
	s_mov_b32 m0, s37
	s_mul_i32 s3, s2, 0x5800
	v_bitop3_b32 v188, v3, v2, v194 bitop3:0xde
	v_or_b32_e32 v2, s83, v1
	s_mul_hi_u32 s37, s40, 0x2c00
	s_add_u32 s38, s59, s3
	s_waitcnt vmcnt(1)
	v_lshlrev_b32_e32 v38, 7, v2
	s_addc_u32 s39, s73, s37
	global_load_dwordx4 v[2:5], v199, s[38:39]
	s_add_i32 s38, s40, 16
	s_add_i32 s41, s3, 0x2c000
	s_mul_hi_u32 s84, s38, 0x2c00
	s_add_u32 s38, s59, s41
	s_addc_u32 s39, s73, s84
	global_load_dwordx4 v[6:9], v199, s[38:39]
	s_add_i32 s38, s40, 32
	s_add_i32 s85, s3, 0x58000
	s_mul_hi_u32 s86, s38, 0x2c00
	s_add_u32 s38, s59, s85
	s_addc_u32 s39, s73, s86
	global_load_dwordx4 v[10:13], v199, s[38:39]
	s_add_i32 s38, s40, 48
	s_add_i32 s87, s3, 0x84000
	s_mul_hi_u32 s88, s38, 0x2c00
	s_add_u32 s38, s59, s87
	s_addc_u32 s39, s73, s88
	global_load_dwordx4 v[14:17], v199, s[38:39]
	s_add_u32 s38, s74, s3
	s_addc_u32 s39, s75, s37
	global_load_dwordx4 v[18:21], v199, s[38:39]
	s_add_u32 s38, s74, s41
	s_addc_u32 s39, s75, s84
	global_load_dwordx4 v[22:25], v199, s[38:39]
	s_add_u32 s38, s74, s85
	s_addc_u32 s39, s75, s86
	global_load_dwordx4 v[26:29], v199, s[38:39]
	s_add_u32 s38, s74, s87
	s_addc_u32 s39, s75, s88
	global_load_dwordx4 v[30:33], v199, s[38:39]
	s_add_i32 s38, s36, 0x8000
	v_add_u32_e32 v39, 0x80, v34
	s_mov_b32 s39, m0
	s_mov_b32 m0, s38
	s_nop 0
	global_load_lds_dwordx4 v39, s[18:19]
	s_mov_b32 m0, s39
	v_add_u32_e32 v39, 0x80, v35
	s_add_i32 s38, s36, 0xa000
	s_mov_b32 s39, m0
	s_mov_b32 m0, s38
	s_nop 0
	global_load_lds_dwordx4 v39, s[18:19]
	s_mov_b32 m0, s39
	v_add_u32_e32 v39, 0x80, v36
	s_add_i32 s38, s36, 0xc000
	s_mov_b32 s39, m0
	s_mov_b32 m0, s38
	s_nop 0
	global_load_lds_dwordx4 v39, s[18:19]
	s_mov_b32 m0, s39
	v_add_u32_e32 v39, 0x80, v37
	s_add_i32 s38, s36, 0xe000
	s_mov_b32 s39, m0
	s_mov_b32 m0, s38
	s_nop 0
	global_load_lds_dwordx4 v39, s[18:19]
	s_mov_b32 m0, s39
	s_waitcnt vmcnt(4)
	v_add_u32_e32 v189, s52, v188
	v_cvt_pk_bf16_f32 v2, v2, v3
	v_cvt_pk_bf16_f32 v3, v4, v5
	v_cvt_pk_bf16_f32 v4, v6, v7
	v_cvt_pk_bf16_f32 v5, v8, v9
	v_or_b32_e32 v186, 0x100, v188
	ds_write2st64_b64 v189, v[2:3], v[4:5] offset1:16
	v_cvt_pk_bf16_f32 v2, v10, v11
	v_cvt_pk_bf16_f32 v3, v12, v13
	v_cvt_pk_bf16_f32 v4, v14, v15
	v_cvt_pk_bf16_f32 v5, v16, v17
	ds_write2st64_b64 v189, v[2:3], v[4:5] offset0:32 offset1:48
	v_cvt_pk_bf16_f32 v2, v18, v19
	v_cvt_pk_bf16_f32 v3, v20, v21
	v_add_u32_e32 v6, s52, v186
	v_cvt_pk_bf16_f32 v4, v22, v23
	v_cvt_pk_bf16_f32 v5, v24, v25
	s_add_i32 s38, s40, 64
	s_add_i32 s41, s3, 0xb0000
	ds_write2st64_b64 v6, v[2:3], v[4:5] offset1:16
	v_cvt_pk_bf16_f32 v2, v26, v27
	v_cvt_pk_bf16_f32 v3, v28, v29
	v_cvt_pk_bf16_f32 v4, v30, v31
	v_cvt_pk_bf16_f32 v5, v32, v33
	s_mul_hi_u32 s84, s38, 0x2c00
	s_add_u32 s38, s59, s41
	ds_write2st64_b64 v6, v[2:3], v[4:5] offset0:32 offset1:48
	s_addc_u32 s39, s73, s84
	global_load_dwordx4 v[30:33], v199, s[38:39]
	s_add_i32 s38, s40, 0x50
	s_add_i32 s85, s3, 0xdc000
	s_mul_hi_u32 s86, s38, 0x2c00
	s_add_u32 s38, s59, s85
	s_addc_u32 s39, s73, s86
	global_load_dwordx4 v[26:29], v199, s[38:39]
	s_add_i32 s38, s40, 0x60
	s_add_i32 s87, s3, 0x108000
	s_mul_hi_u32 s88, s38, 0x2c00
	s_add_u32 s38, s59, s87
	s_addc_u32 s39, s73, s88
	s_addk_i32 s40, 0x70
	s_add_i32 s89, s3, 0x134000
	global_load_dwordx4 v[22:25], v199, s[38:39]
	s_mul_hi_u32 s40, s40, 0x2c00
	s_add_u32 s38, s59, s89
	s_addc_u32 s39, s73, s40
	global_load_dwordx4 v[18:21], v199, s[38:39]
	s_add_u32 s38, s74, s41
	s_addc_u32 s39, s75, s84
	global_load_dwordx4 v[14:17], v199, s[38:39]
	s_add_u32 s38, s74, s85
	s_addc_u32 s39, s75, s86
	global_load_dwordx4 v[10:13], v199, s[38:39]
	s_add_u32 s38, s74, s87
	s_addc_u32 s39, s75, s88
	global_load_dwordx4 v[6:9], v199, s[38:39]
	s_add_u32 s38, s74, s89
	s_addc_u32 s39, s75, s40
	global_load_dwordx4 v[2:5], v199, s[38:39]
	s_mul_hi_u32 s2, s2, 0x5800
	s_add_u32 s38, s74, s3
	s_waitcnt lgkmcnt(0)
	s_barrier
	s_addc_u32 s39, s75, s2
	s_add_u32 s40, s59, s3
	v_add_u32_e32 v215, 0x100, v34
	v_mov_b32_e32 v34, 0
	v_or_b32_e32 v183, v38, v196
	s_mov_b32 s37, 0x8000
	v_or_b32_e32 v187, v38, v197
	s_addc_u32 s41, s73, s2
	v_add_u32_e32 v212, 0x100, v37
	v_add_u32_e32 v213, 0x100, v36
	v_add_u32_e32 v214, 0x100, v35
	s_mov_b32 s84, 0x10000
	s_mov_b32 s85, 0
	s_mov_b64 s[2:3], 0
	v_mov_b32_e32 v35, v34
	v_mov_b32_e32 v36, v34
	v_mov_b32_e32 v37, v34
	v_mov_b32_e32 v38, v34
	v_mov_b32_e32 v39, v34
	v_mov_b32_e32 v40, v34
	v_mov_b32_e32 v41, v34
	v_mov_b32_e32 v46, v34
	v_mov_b32_e32 v47, v34
	v_mov_b32_e32 v48, v34
	v_mov_b32_e32 v49, v34
	v_mov_b32_e32 v50, v34
	v_mov_b32_e32 v51, v34
	v_mov_b32_e32 v52, v34
	v_mov_b32_e32 v53, v34
	s_waitcnt vmcnt(12)
	v_mov_b32_e32 v42, v34
	v_mov_b32_e32 v43, v34
	v_mov_b32_e32 v44, v34
	v_mov_b32_e32 v45, v34
	v_mov_b32_e32 v54, v34
	v_mov_b32_e32 v55, v34
	v_mov_b32_e32 v56, v34
	v_mov_b32_e32 v57, v34
	v_mov_b32_e32 v58, v34
	v_mov_b32_e32 v59, v34
	v_mov_b32_e32 v60, v34
	v_mov_b32_e32 v61, v34
	v_mov_b32_e32 v62, v34
	v_mov_b32_e32 v63, v34
	v_mov_b32_e32 v64, v34
	v_mov_b32_e32 v65, v34
	v_mov_b32_e32 v66, v34
	v_mov_b32_e32 v67, v34
	v_mov_b32_e32 v68, v34
	v_mov_b32_e32 v69, v34
	v_mov_b32_e32 v70, v34
	v_mov_b32_e32 v71, v34
	v_mov_b32_e32 v72, v34
	v_mov_b32_e32 v73, v34
	v_mov_b32_e32 v74, v34
	v_mov_b32_e32 v75, v34
	v_mov_b32_e32 v76, v34
	v_mov_b32_e32 v77, v34
	v_mov_b32_e32 v78, v34
	v_mov_b32_e32 v79, v34
	v_mov_b32_e32 v80, v34
	v_mov_b32_e32 v81, v34
	v_mov_b32_e32 v82, v34
	v_mov_b32_e32 v83, v34
	v_mov_b32_e32 v84, v34
	v_mov_b32_e32 v85, v34
	v_mov_b32_e32 v86, v34
	v_mov_b32_e32 v87, v34
	v_mov_b32_e32 v88, v34
	v_mov_b32_e32 v89, v34
	v_mov_b32_e32 v90, v34
	v_mov_b32_e32 v91, v34
	v_mov_b32_e32 v92, v34
	v_mov_b32_e32 v93, v34
	v_mov_b32_e32 v94, v34
	v_mov_b32_e32 v95, v34
	v_mov_b32_e32 v96, v34
	v_mov_b32_e32 v97, v34
	v_mov_b32_e32 v98, v34
	v_mov_b32_e32 v99, v34
	v_mov_b32_e32 v100, v34
	v_mov_b32_e32 v101, v34
	v_mov_b32_e32 v102, v34
	v_mov_b32_e32 v103, v34
	v_mov_b32_e32 v104, v34
	v_mov_b32_e32 v105, v34
	v_mov_b32_e32 v106, v34
	v_mov_b32_e32 v107, v34
	v_mov_b32_e32 v108, v34
	v_mov_b32_e32 v109, v34
	v_mov_b32_e32 v110, v34
	v_mov_b32_e32 v111, v34
	v_mov_b32_e32 v112, v34
	v_mov_b32_e32 v113, v34
	v_mov_b32_e32 v114, v34
	v_mov_b32_e32 v115, v34
	v_mov_b32_e32 v116, v34
	v_mov_b32_e32 v117, v34
	v_mov_b32_e32 v118, v34
	v_mov_b32_e32 v119, v34
	v_mov_b32_e32 v120, v34
	v_mov_b32_e32 v121, v34
	v_mov_b32_e32 v122, v34
	v_mov_b32_e32 v123, v34
	v_mov_b32_e32 v124, v34
	v_mov_b32_e32 v125, v34
	v_mov_b32_e32 v126, v34
	v_mov_b32_e32 v127, v34
	v_mov_b32_e32 v128, v34
	v_mov_b32_e32 v129, v34
	v_mov_b32_e32 v130, v34
	v_mov_b32_e32 v131, v34
	v_mov_b32_e32 v132, v34
	v_mov_b32_e32 v133, v34
	v_mov_b32_e32 v134, v34
	v_mov_b32_e32 v135, v34
	v_mov_b32_e32 v136, v34
	v_mov_b32_e32 v137, v34
	v_mov_b32_e32 v138, v34
	v_mov_b32_e32 v139, v34
	v_mov_b32_e32 v140, v34
	v_mov_b32_e32 v141, v34
	v_mov_b32_e32 v142, v34
	v_mov_b32_e32 v143, v34
	v_mov_b32_e32 v144, v34
	v_mov_b32_e32 v145, v34
	v_mov_b32_e32 v146, v34
	v_mov_b32_e32 v147, v34
	v_mov_b32_e32 v148, v34
	v_mov_b32_e32 v149, v34
	v_mov_b32_e32 v150, v34
	v_mov_b32_e32 v151, v34
	v_mov_b32_e32 v152, v34
	v_mov_b32_e32 v153, v34
	v_mov_b32_e32 v154, v34
	v_mov_b32_e32 v155, v34
	v_mov_b32_e32 v156, v34
	v_mov_b32_e32 v157, v34
	v_mov_b32_e32 v158, v34
	v_mov_b32_e32 v159, v34
	v_mov_b32_e32 v160, v34
	v_mov_b32_e32 v161, v34

.LBB0_1477:
	s_add_u32 s2, s59, 0xc60000
	s_addc_u32 s3, s73, 0
	s_add_u32 s35, s74, 0xc60000
	s_addc_u32 s36, s75, 0
	s_lshr_b32 s37, s33, 6
	s_lshl_b32 s39, s37, 1
	s_bfe_u32 s4, s33, 0x20006
	v_or_b32_e32 v2, s39, v193
	s_and_b32 s5, s37, 4
	v_and_or_b32 v3, v2, 3, s5
	s_lshr_b32 s5, s33, 1
	s_lshl_b32 s33, s4, 6
	s_or_b32 s34, s33, 32
	v_bitop3_b32 v184, s33, v203, v198 bitop3:0xde
	v_bitop3_b32 v183, s34, v203, v198 bitop3:0xde
	s_or_b32 s34, s33, 0x100
	s_or_b32 s33, s33, 0x120
	v_bitop3_b32 v172, s33, v203, v198 bitop3:0xde
	s_lshl_b32 s33, s37, 10
	v_bitop3_b32 v181, s34, v203, v198 bitop3:0xde
	s_add_i32 s33, s33, 0
	s_mov_b32 s34, m0
	s_mov_b32 m0, s33
	s_nop 0
	global_load_lds_dwordx4 v208, s[18:19]
	s_mov_b32 m0, s34
	s_add_i32 s34, s33, 0x2000
	s_mov_b32 s38, m0
	s_mov_b32 m0, s34
	s_nop 0
	global_load_lds_dwordx4 v209, s[18:19]
	s_mov_b32 m0, s38
	s_add_i32 s34, s33, 0x4000
	s_mov_b32 s38, m0
	s_mov_b32 m0, s34
	s_nop 0
	global_load_lds_dwordx4 v210, s[18:19]
	s_mov_b32 m0, s38
	s_add_i32 s34, s33, 0x6000
	s_mov_b32 s38, m0
	s_mov_b32 m0, s34
	s_nop 0
	global_load_lds_dwordx4 v211, s[18:19]
	s_mov_b32 m0, s38
	v_lshlrev_b32_e32 v2, 9, v2
	v_lshlrev_b32_e32 v3, 5, v3
	s_and_b32 s5, s5, 0x7fffff80
	s_mul_i32 s38, s37, 0x5800
	v_bitop3_b32 v186, v3, v2, v194 bitop3:0xde
	v_or_b32_e32 v2, s5, v1
	s_mul_hi_u32 s34, s39, 0x2c00
	s_add_u32 s40, s2, s38
	v_lshlrev_b32_e32 v34, 7, v2
	s_addc_u32 s41, s3, s34
	global_load_dwordx4 v[2:5], v199, s[40:41]
	s_add_i32 s40, s39, 16
	s_add_i32 s59, s38, 0x2c000
	s_mul_hi_u32 s73, s40, 0x2c00
	s_add_u32 s40, s2, s59
	s_addc_u32 s41, s3, s73
	global_load_dwordx4 v[6:9], v199, s[40:41]
	s_add_i32 s40, s39, 32
	s_add_i32 s74, s38, 0x58000
	s_mul_hi_u32 s75, s40, 0x2c00
	s_add_u32 s40, s2, s74
	s_addc_u32 s41, s3, s75
	s_waitcnt vmcnt(6)
	global_load_dwordx4 v[10:13], v199, s[40:41]
	s_add_i32 s40, s39, 48
	s_add_i32 s78, s38, 0x84000
	s_mul_hi_u32 s79, s40, 0x2c00
	s_add_u32 s40, s2, s78
	s_addc_u32 s41, s3, s79
	s_waitcnt vmcnt(5)
	global_load_dwordx4 v[14:17], v199, s[40:41]
	s_add_u32 s40, s35, s38
	s_addc_u32 s41, s36, s34
	s_waitcnt vmcnt(4)
	global_load_dwordx4 v[18:21], v199, s[40:41]
	s_add_u32 s40, s35, s59
	s_addc_u32 s41, s36, s73
	s_waitcnt vmcnt(3)
	global_load_dwordx4 v[22:25], v199, s[40:41]
	s_add_u32 s40, s35, s74
	s_addc_u32 s41, s36, s75
	s_waitcnt vmcnt(2)
	global_load_dwordx4 v[26:29], v199, s[40:41]
	s_add_u32 s40, s35, s78
	s_addc_u32 s41, s36, s79
	global_load_dwordx4 v[30:33], v199, s[40:41]
	s_add_i32 s40, s33, 0x8000
	v_add_u32_e32 v35, 0x80, v208
	s_mov_b32 s41, m0
	s_mov_b32 m0, s40
	s_nop 0
	global_load_lds_dwordx4 v35, s[18:19]
	s_mov_b32 m0, s41
	v_add_u32_e32 v35, 0x80, v209
	s_add_i32 s40, s33, 0xa000
	s_mov_b32 s41, m0
	s_mov_b32 m0, s40
	s_nop 0
	global_load_lds_dwordx4 v35, s[18:19]
	s_mov_b32 m0, s41
	v_add_u32_e32 v35, 0x80, v210
	s_add_i32 s40, s33, 0xc000
	s_mov_b32 s41, m0
	s_mov_b32 m0, s40
	s_nop 0
	global_load_lds_dwordx4 v35, s[18:19]
	s_mov_b32 m0, s41
	v_add_u32_e32 v35, 0x80, v211
	s_add_i32 s40, s33, 0xe000
	s_mov_b32 s41, m0
	s_mov_b32 m0, s40
	s_nop 0
	global_load_lds_dwordx4 v35, s[18:19]
	s_mov_b32 m0, s41
	s_waitcnt vmcnt(4)
	v_add_u32_e32 v189, s52, v186
	v_cvt_pk_bf16_f32 v2, v2, v3
	v_cvt_pk_bf16_f32 v3, v4, v5
	v_cvt_pk_bf16_f32 v4, v6, v7
	v_cvt_pk_bf16_f32 v5, v8, v9
	v_or_b32_e32 v185, 0x100, v186
	ds_write2st64_b64 v189, v[2:3], v[4:5] offset1:16
	v_cvt_pk_bf16_f32 v2, v10, v11
	v_cvt_pk_bf16_f32 v3, v12, v13
	v_cvt_pk_bf16_f32 v4, v14, v15
	v_cvt_pk_bf16_f32 v5, v16, v17
	ds_write2st64_b64 v189, v[2:3], v[4:5] offset0:32 offset1:48
	v_cvt_pk_bf16_f32 v2, v18, v19
	v_cvt_pk_bf16_f32 v3, v20, v21
	v_add_u32_e32 v6, s52, v185
	v_cvt_pk_bf16_f32 v4, v22, v23
	v_cvt_pk_bf16_f32 v5, v24, v25
	s_add_i32 s40, s39, 64
	s_add_i32 s59, s38, 0xb0000
	ds_write2st64_b64 v6, v[2:3], v[4:5] offset1:16
	v_cvt_pk_bf16_f32 v2, v26, v27
	v_cvt_pk_bf16_f32 v3, v28, v29
	v_cvt_pk_bf16_f32 v4, v30, v31
	v_cvt_pk_bf16_f32 v5, v32, v33
	s_mul_hi_u32 s73, s40, 0x2c00
	s_add_u32 s40, s2, s59
	ds_write2st64_b64 v6, v[2:3], v[4:5] offset0:32 offset1:48
	s_addc_u32 s41, s3, s73
	global_load_dwordx4 v[30:33], v199, s[40:41]
	s_add_i32 s40, s39, 0x50
	s_add_i32 s74, s38, 0xdc000
	s_mul_hi_u32 s75, s40, 0x2c00
	s_add_u32 s40, s2, s74
	s_addc_u32 s41, s3, s75
	global_load_dwordx4 v[26:29], v199, s[40:41]
	s_add_i32 s40, s39, 0x60
	s_add_i32 s78, s38, 0x108000
	s_mul_hi_u32 s79, s40, 0x2c00
	s_add_u32 s40, s2, s78
	s_addc_u32 s41, s3, s79
	s_addk_i32 s39, 0x70
	s_add_i32 s83, s38, 0x134000
	global_load_dwordx4 v[22:25], v199, s[40:41]
	s_mul_hi_u32 s39, s39, 0x2c00
	s_add_u32 s40, s2, s83
	s_addc_u32 s41, s3, s39
	global_load_dwordx4 v[18:21], v199, s[40:41]
	s_add_u32 s40, s35, s59
	s_addc_u32 s41, s36, s73
	global_load_dwordx4 v[14:17], v199, s[40:41]
	s_add_u32 s40, s35, s74
	s_addc_u32 s41, s36, s75
	global_load_dwordx4 v[10:13], v199, s[40:41]
	s_add_u32 s40, s35, s78
	s_addc_u32 s41, s36, s79
	global_load_dwordx4 v[6:9], v199, s[40:41]
	s_add_u32 s40, s35, s83
	s_addc_u32 s41, s36, s39
	s_mul_hi_u32 s39, s37, 0x5800
	s_add_u32 s35, s35, s38
	global_load_dwordx4 v[2:5], v199, s[40:41]
	s_waitcnt lgkmcnt(0)
	s_barrier
	s_addc_u32 s36, s36, s39
	v_or_b32_e32 v187, v34, v196
	v_or_b32_e32 v188, v34, v197
	s_add_u32 s37, s2, s38
	v_mov_b32_e32 v34, 0
	s_mov_b32 s34, 0x8000
	s_addc_u32 s38, s3, s39
	v_add_u32_e32 v211, 0x100, v211
	v_add_u32_e32 v210, 0x100, v210
	v_add_u32_e32 v209, 0x100, v209
	v_add_u32_e32 v208, 0x100, v208
	s_mov_b32 s39, 0x10000
	s_mov_b32 s40, 0
	s_mov_b64 s[2:3], 0
	v_mov_b32_e32 v35, v34
	v_mov_b32_e32 v36, v34
	v_mov_b32_e32 v37, v34
	s_waitcnt vmcnt(12)
	v_mov_b32_e32 v38, v34
	v_mov_b32_e32 v39, v34
	v_mov_b32_e32 v40, v34
	v_mov_b32_e32 v41, v34
	v_mov_b32_e32 v46, v34
	v_mov_b32_e32 v47, v34
	v_mov_b32_e32 v48, v34
	v_mov_b32_e32 v49, v34
	v_mov_b32_e32 v50, v34
	v_mov_b32_e32 v51, v34
	v_mov_b32_e32 v52, v34
	v_mov_b32_e32 v53, v34
	s_waitcnt vmcnt(12)
	v_mov_b32_e32 v42, v34
	v_mov_b32_e32 v43, v34
	v_mov_b32_e32 v44, v34
	v_mov_b32_e32 v45, v34
	v_mov_b32_e32 v54, v34
	v_mov_b32_e32 v55, v34
	v_mov_b32_e32 v56, v34
	v_mov_b32_e32 v57, v34
	v_mov_b32_e32 v58, v34
	v_mov_b32_e32 v59, v34
	v_mov_b32_e32 v60, v34
	v_mov_b32_e32 v61, v34
	v_mov_b32_e32 v62, v34
	v_mov_b32_e32 v63, v34
	v_mov_b32_e32 v64, v34
	v_mov_b32_e32 v65, v34
	v_mov_b32_e32 v66, v34
	v_mov_b32_e32 v67, v34
	v_mov_b32_e32 v68, v34
	v_mov_b32_e32 v69, v34
	v_mov_b32_e32 v70, v34
	v_mov_b32_e32 v71, v34
	v_mov_b32_e32 v72, v34
	v_mov_b32_e32 v73, v34
	v_mov_b32_e32 v74, v34
	v_mov_b32_e32 v75, v34
	v_mov_b32_e32 v76, v34
	v_mov_b32_e32 v77, v34
	v_mov_b32_e32 v78, v34
	v_mov_b32_e32 v79, v34
	v_mov_b32_e32 v80, v34
	v_mov_b32_e32 v81, v34
	v_mov_b32_e32 v82, v34
	v_mov_b32_e32 v83, v34
	v_mov_b32_e32 v84, v34
	v_mov_b32_e32 v85, v34
	v_mov_b32_e32 v86, v34
	v_mov_b32_e32 v87, v34
	v_mov_b32_e32 v88, v34
	v_mov_b32_e32 v89, v34
	v_mov_b32_e32 v90, v34
	v_mov_b32_e32 v91, v34
	v_mov_b32_e32 v92, v34
	v_mov_b32_e32 v93, v34
	v_mov_b32_e32 v94, v34
	v_mov_b32_e32 v95, v34
	v_mov_b32_e32 v96, v34
	v_mov_b32_e32 v97, v34
	v_mov_b32_e32 v98, v34
	v_mov_b32_e32 v99, v34
	v_mov_b32_e32 v100, v34
	v_mov_b32_e32 v101, v34
	v_mov_b32_e32 v102, v34
	v_mov_b32_e32 v103, v34
	v_mov_b32_e32 v104, v34
	v_mov_b32_e32 v105, v34
	v_mov_b32_e32 v106, v34
	v_mov_b32_e32 v107, v34
	v_mov_b32_e32 v108, v34
	v_mov_b32_e32 v109, v34
	v_mov_b32_e32 v110, v34
	v_mov_b32_e32 v111, v34
	v_mov_b32_e32 v112, v34
	v_mov_b32_e32 v113, v34
	v_mov_b32_e32 v114, v34
	v_mov_b32_e32 v115, v34
	v_mov_b32_e32 v116, v34
	v_mov_b32_e32 v117, v34
	v_mov_b32_e32 v118, v34
	v_mov_b32_e32 v119, v34
	v_mov_b32_e32 v120, v34
	v_mov_b32_e32 v121, v34
	v_mov_b32_e32 v122, v34
	v_mov_b32_e32 v123, v34
	v_mov_b32_e32 v124, v34
	v_mov_b32_e32 v125, v34
	v_mov_b32_e32 v126, v34
	v_mov_b32_e32 v127, v34
	v_mov_b32_e32 v128, v34
	v_mov_b32_e32 v129, v34
	v_mov_b32_e32 v130, v34
	v_mov_b32_e32 v131, v34
	v_mov_b32_e32 v132, v34
	v_mov_b32_e32 v133, v34
	v_mov_b32_e32 v134, v34
	v_mov_b32_e32 v135, v34
	v_mov_b32_e32 v136, v34
	v_mov_b32_e32 v137, v34
	v_mov_b32_e32 v138, v34
	v_mov_b32_e32 v139, v34
	v_mov_b32_e32 v140, v34
	v_mov_b32_e32 v141, v34
	v_mov_b32_e32 v142, v34
	v_mov_b32_e32 v143, v34
	v_mov_b32_e32 v144, v34
	v_mov_b32_e32 v145, v34
	v_mov_b32_e32 v146, v34
	v_mov_b32_e32 v147, v34
	v_mov_b32_e32 v148, v34
	v_mov_b32_e32 v149, v34
	v_mov_b32_e32 v150, v34
	v_mov_b32_e32 v151, v34
	v_mov_b32_e32 v152, v34
	v_mov_b32_e32 v153, v34
	v_mov_b32_e32 v154, v34
	v_mov_b32_e32 v155, v34
	v_mov_b32_e32 v156, v34
	v_mov_b32_e32 v157, v34
	v_mov_b32_e32 v158, v34
	v_mov_b32_e32 v159, v34
	v_mov_b32_e32 v160, v34
	v_mov_b32_e32 v161, v34

.LBB0_1539:
	s_ashr_i32 s10, s16, 5
	s_ashr_i32 s11, s10, 31
	s_mul_i32 s14, s10, 0x580000
	s_mul_hi_i32 s2, s10, 0x580000
	s_add_u32 s14, s19, s14
	s_addc_u32 s15, s20, s2
	s_mul_i32 s17, s10, 0x1600000
	s_mul_hi_i32 s2, s10, 0x1600000
	s_add_u32 s17, s64, s17
	s_addc_u32 s2, s65, s2
	s_lshl_b32 s30, s16, 6
	s_and_b32 s30, s30, 0x700
	s_lshl_b32 s31, s30, 2
	s_add_u32 s17, s17, s31
	s_addc_u32 s38, s2, 0
	s_lshl_b32 s2, s16, 8
	v_readfirstlane_b32 s16, v0
	s_and_b32 s31, s2, 0x300
	s_lshr_b32 s2, s16, 6
	s_lshl_b32 s34, s2, 9
	s_lshl_b32 s33, s2, 5
	s_and_b32 s35, s33, 0x60
	v_mov_b32_e32 v3, s34
	s_lshr_b32 s34, s16, 1
	v_bitop3_b32 v206, s35, v3, v194 bitop3:0xde
	s_and_b32 s35, s34, 0x7fffff80
	s_lshl_b32 s34, s16, 1
	s_and_b32 s34, s34, 0x180
	s_or_b32 s36, s34, 32
	v_or_b32_e32 v2, s31, v171
	v_bitop3_b32 v181, s36, v201, v198 bitop3:0xde
	s_or_b32 s36, s34, 64
	v_mul_u32_u24_e32 v34, 0xb00, v2
	v_bitop3_b32 v179, s36, v201, v198 bitop3:0xde
	s_or_b32 s36, s34, 0x60
	v_or_b32_e32 v2, v34, v177
	v_bitop3_b32 v172, s36, v201, v198 bitop3:0xde
	s_lshl_b32 s36, s2, 10
	v_lshlrev_b32_e32 v35, 1, v2
	s_add_i32 s36, s36, 0
	s_mov_b32 s37, m0
	s_mov_b32 m0, s36
	s_nop 0
	global_load_lds_dwordx4 v35, s[14:15]
	s_mov_b32 m0, s37
	s_add_i32 s37, s36, 0x2000
	v_add_lshl_u32 v36, v190, v34, 1
	s_mov_b32 s39, m0
	s_mov_b32 m0, s37
	s_nop 0
	global_load_lds_dwordx4 v36, s[14:15]
	s_mov_b32 m0, s39
	s_add_i32 s37, s36, 0x4000
	v_add_lshl_u32 v37, v191, v34, 1
	s_mov_b32 s39, m0
	s_mov_b32 m0, s37
	s_nop 0
	global_load_lds_dwordx4 v37, s[14:15]
	s_mov_b32 m0, s39
	s_add_i32 s37, s36, 0x6000
	s_lshl_b64 s[40:41], s[2:3], 13
	s_add_u32 s40, s17, s40
	v_bitop3_b32 v2, s33, v194, v203 bitop3:0x6c
	v_or_b32_e32 v4, s35, v1
	s_addc_u32 s41, s38, s41
	s_waitcnt vmcnt(1)
	v_add_lshl_u32 v38, v192, v34, 1
	v_lshlrev_b32_e32 v39, 7, v4
	v_bitop3_b32 v205, v2, s23, v3 bitop3:0x36
	s_mov_b32 s39, m0
	s_mov_b32 m0, s37
	s_nop 0
	global_load_lds_dwordx4 v38, s[14:15]
	s_mov_b32 m0, s39
	global_load_dwordx4 v[2:5], v199, s[40:41]
	s_add_i32 s40, s2, 8
	s_mov_b32 s41, s3
	s_lshl_b64 s[40:41], s[40:41], 13
	s_add_u32 s40, s17, s40
	s_addc_u32 s41, s38, s41
	global_load_dwordx4 v[6:9], v199, s[40:41]
	s_add_i32 s40, s2, 16
	s_mov_b32 s41, s3
	s_lshl_b64 s[40:41], s[40:41], 13
	s_add_u32 s40, s17, s40
	s_addc_u32 s41, s38, s41
	global_load_dwordx4 v[10:13], v199, s[40:41]
	s_add_i32 s40, s2, 24
	s_mov_b32 s41, s3
	s_lshl_b64 s[40:41], s[40:41], 13
	s_add_u32 s40, s17, s40
	s_addc_u32 s41, s38, s41
	global_load_dwordx4 v[14:17], v199, s[40:41]
	s_add_i32 s40, s2, 32
	s_mov_b32 s41, s3
	s_lshl_b64 s[40:41], s[40:41], 13
	s_add_u32 s40, s17, s40
	s_addc_u32 s41, s38, s41
	global_load_dwordx4 v[18:21], v199, s[40:41]
	s_add_i32 s40, s2, 40
	s_mov_b32 s41, s3
	s_lshl_b64 s[40:41], s[40:41], 13
	s_add_u32 s40, s17, s40
	s_addc_u32 s41, s38, s41
	global_load_dwordx4 v[22:25], v199, s[40:41]
	s_add_i32 s40, s2, 48
	s_mov_b32 s41, s3
	s_lshl_b64 s[40:41], s[40:41], 13
	s_add_u32 s40, s17, s40
	s_addc_u32 s41, s38, s41
	global_load_dwordx4 v[26:29], v199, s[40:41]
	s_add_i32 s40, s2, 56
	s_mov_b32 s41, s3
	s_lshl_b64 s[40:41], s[40:41], 13
	s_add_u32 s40, s17, s40
	s_addc_u32 s41, s38, s41
	s_add_i32 s39, s36, 0x8000
	v_or_b32_e32 v35, 0x80, v35
	global_load_dwordx4 v[30:33], v199, s[40:41]
	s_mov_b32 s40, m0
	s_mov_b32 m0, s39
	s_nop 0
	global_load_lds_dwordx4 v35, s[14:15]
	s_mov_b32 m0, s40
	v_or_b32_e32 v35, 0x80, v36
	s_add_i32 s39, s36, 0xa000
	s_mov_b32 s40, m0
	s_mov_b32 m0, s39
	s_nop 0
	global_load_lds_dwordx4 v35, s[14:15]
	s_mov_b32 m0, s40
	v_or_b32_e32 v35, 0x80, v37
	s_add_i32 s39, s36, 0xc000
	s_mov_b32 s40, m0
	s_mov_b32 m0, s39
	s_nop 0
	global_load_lds_dwordx4 v35, s[14:15]
	s_mov_b32 m0, s40
	v_or_b32_e32 v35, 0x80, v38
	s_add_i32 s39, s36, 0xe000
	s_mov_b32 s40, m0
	s_mov_b32 m0, s39
	s_nop 0
	global_load_lds_dwordx4 v35, s[14:15]
	s_mov_b32 m0, s40
	s_waitcnt vmcnt(4)
	s_add_i32 s40, s2, 64
	v_cvt_pk_bf16_f32 v2, v2, v3
	v_cvt_pk_bf16_f32 v3, v4, v5
	v_add_u32_e32 v4, s24, v206
	ds_write_b64 v4, v[2:3]
	v_cvt_pk_bf16_f32 v2, v6, v7
	v_cvt_pk_bf16_f32 v3, v8, v9
	v_add_u32_e32 v5, s24, v205
	ds_write_b64 v5, v[2:3] offset:4096
	v_cvt_pk_bf16_f32 v2, v10, v11
	v_cvt_pk_bf16_f32 v3, v12, v13
	ds_write_b64 v4, v[2:3] offset:8192
	v_cvt_pk_bf16_f32 v2, v14, v15
	v_cvt_pk_bf16_f32 v3, v16, v17
	ds_write_b64 v5, v[2:3] offset:12288
	v_cvt_pk_bf16_f32 v2, v18, v19
	v_cvt_pk_bf16_f32 v3, v20, v21
	s_mov_b32 s41, s3
	ds_write_b64 v4, v[2:3] offset:16384
	v_cvt_pk_bf16_f32 v2, v22, v23
	v_cvt_pk_bf16_f32 v3, v24, v25
	s_lshl_b64 s[40:41], s[40:41], 13
	ds_write_b64 v5, v[2:3] offset:20480
	v_cvt_pk_bf16_f32 v2, v26, v27
	v_cvt_pk_bf16_f32 v3, v28, v29
	s_add_u32 s40, s17, s40
	ds_write_b64 v4, v[2:3] offset:24576
	v_cvt_pk_bf16_f32 v2, v30, v31
	v_cvt_pk_bf16_f32 v3, v32, v33
	s_addc_u32 s41, s38, s41
	ds_write_b64 v5, v[2:3] offset:28672
	global_load_dwordx4 v[30:33], v199, s[40:41]
	s_add_i32 s40, s2, 0x48
	s_mov_b32 s41, s3
	s_lshl_b64 s[40:41], s[40:41], 13
	s_add_u32 s40, s17, s40
	s_addc_u32 s41, s38, s41
	global_load_dwordx4 v[26:29], v199, s[40:41]
	s_add_i32 s40, s2, 0x50
	s_mov_b32 s41, s3
	s_lshl_b64 s[40:41], s[40:41], 13
	s_add_u32 s40, s17, s40
	s_addc_u32 s41, s38, s41
	global_load_dwordx4 v[22:25], v199, s[40:41]
	s_add_i32 s40, s2, 0x58
	s_mov_b32 s41, s3
	s_lshl_b64 s[40:41], s[40:41], 13
	s_add_u32 s40, s17, s40
	s_addc_u32 s41, s38, s41
	global_load_dwordx4 v[18:21], v199, s[40:41]
	s_add_i32 s40, s2, 0x60
	s_mov_b32 s41, s3
	s_lshl_b64 s[40:41], s[40:41], 13
	s_add_u32 s40, s17, s40
	s_addc_u32 s41, s38, s41
	global_load_dwordx4 v[14:17], v199, s[40:41]
	s_add_i32 s40, s2, 0x68
	s_mov_b32 s41, s3
	s_lshl_b64 s[40:41], s[40:41], 13
	s_add_u32 s40, s17, s40
	s_addc_u32 s41, s38, s41
	global_load_dwordx4 v[10:13], v199, s[40:41]
	s_add_i32 s40, s2, 0x70
	s_mov_b32 s41, s3
	s_lshl_b64 s[40:41], s[40:41], 13
	s_add_u32 s40, s17, s40
	s_addc_u32 s41, s38, s41
	s_addk_i32 s2, 0x78
	global_load_dwordx4 v[6:9], v199, s[40:41]
	s_lshl_b64 s[40:41], s[2:3], 13
	s_add_u32 s40, s17, s40
	s_addc_u32 s41, s38, s41
	global_load_dwordx4 v[2:5], v199, s[40:41]
	s_lshl_b64 s[40:41], s[16:17], 7
	s_waitcnt lgkmcnt(0)
	s_barrier
	s_and_b32 s16, s41, 0x7f
	s_and_b32 s2, s40, 0xffffe000
	s_add_u32 s2, s17, s2
	v_lshl_add_u32 v209, v34, 1, v202
	v_mov_b32_e32 v34, 0
	v_bitop3_b32 v183, s34, v201, v198 bitop3:0xde
	v_or_b32_e32 v207, v39, v196
	s_mov_b32 s37, 0x8000
	v_or_b32_e32 v208, v39, v197
	s_addc_u32 s38, s38, s16
	s_mov_b32 s39, 0x10000
	s_mov_b32 s40, 0
	s_mov_b64 s[16:17], 0
	v_mov_b32_e32 v35, v34
	v_mov_b32_e32 v36, v34
	v_mov_b32_e32 v37, v34
	v_mov_b32_e32 v38, v34
	v_mov_b32_e32 v39, v34
	v_mov_b32_e32 v40, v34
	v_mov_b32_e32 v41, v34
	s_waitcnt vmcnt(12)
	v_mov_b32_e32 v42, v34
	v_mov_b32_e32 v43, v34
	v_mov_b32_e32 v44, v34
	v_mov_b32_e32 v45, v34
	v_mov_b32_e32 v46, v34
	v_mov_b32_e32 v47, v34
	v_mov_b32_e32 v48, v34
	v_mov_b32_e32 v49, v34
	v_mov_b32_e32 v50, v34
	v_mov_b32_e32 v51, v34
	v_mov_b32_e32 v52, v34
	v_mov_b32_e32 v53, v34
	v_mov_b32_e32 v54, v34
	v_mov_b32_e32 v55, v34
	v_mov_b32_e32 v56, v34
	v_mov_b32_e32 v57, v34
	v_mov_b32_e32 v58, v34
	v_mov_b32_e32 v59, v34
	v_mov_b32_e32 v60, v34
	v_mov_b32_e32 v61, v34
	v_mov_b32_e32 v62, v34
	v_mov_b32_e32 v63, v34
	v_mov_b32_e32 v64, v34
	v_mov_b32_e32 v65, v34
	v_mov_b32_e32 v66, v34
	v_mov_b32_e32 v67, v34
	v_mov_b32_e32 v68, v34
	v_mov_b32_e32 v69, v34
	v_mov_b32_e32 v70, v34
	v_mov_b32_e32 v71, v34
	v_mov_b32_e32 v72, v34
	v_mov_b32_e32 v73, v34
	v_mov_b32_e32 v74, v34
	v_mov_b32_e32 v75, v34
	v_mov_b32_e32 v76, v34
	v_mov_b32_e32 v77, v34
	v_mov_b32_e32 v78, v34
	v_mov_b32_e32 v79, v34
	v_mov_b32_e32 v80, v34
	v_mov_b32_e32 v81, v34
	v_mov_b32_e32 v82, v34
	v_mov_b32_e32 v83, v34
	v_mov_b32_e32 v84, v34
	v_mov_b32_e32 v85, v34
	v_mov_b32_e32 v86, v34
	v_mov_b32_e32 v87, v34
	v_mov_b32_e32 v88, v34
	v_mov_b32_e32 v89, v34
	v_mov_b32_e32 v90, v34
	v_mov_b32_e32 v91, v34
	v_mov_b32_e32 v92, v34
	v_mov_b32_e32 v93, v34
	v_mov_b32_e32 v94, v34
	v_mov_b32_e32 v95, v34
	v_mov_b32_e32 v96, v34
	v_mov_b32_e32 v97, v34
	v_mov_b32_e32 v98, v34
	v_mov_b32_e32 v99, v34
	v_mov_b32_e32 v100, v34
	v_mov_b32_e32 v101, v34
	v_mov_b32_e32 v102, v34
	v_mov_b32_e32 v103, v34
	v_mov_b32_e32 v104, v34
	v_mov_b32_e32 v105, v34
	v_mov_b32_e32 v106, v34
	v_mov_b32_e32 v107, v34
	v_mov_b32_e32 v108, v34
	v_mov_b32_e32 v109, v34
	v_mov_b32_e32 v110, v34
	v_mov_b32_e32 v111, v34
	v_mov_b32_e32 v112, v34
	v_mov_b32_e32 v113, v34
	v_mov_b32_e32 v114, v34
	v_mov_b32_e32 v115, v34
	v_mov_b32_e32 v116, v34
	v_mov_b32_e32 v117, v34
	v_mov_b32_e32 v118, v34
	v_mov_b32_e32 v119, v34
	v_mov_b32_e32 v120, v34
	v_mov_b32_e32 v121, v34
	v_mov_b32_e32 v122, v34
	v_mov_b32_e32 v123, v34
	v_mov_b32_e32 v124, v34
	v_mov_b32_e32 v125, v34
	v_mov_b32_e32 v126, v34
	v_mov_b32_e32 v127, v34
	v_mov_b32_e32 v128, v34
	v_mov_b32_e32 v129, v34
	v_mov_b32_e32 v130, v34
	v_mov_b32_e32 v131, v34
	v_mov_b32_e32 v132, v34
	v_mov_b32_e32 v133, v34
	v_mov_b32_e32 v134, v34
	v_mov_b32_e32 v135, v34
	v_mov_b32_e32 v136, v34
	v_mov_b32_e32 v137, v34
	v_mov_b32_e32 v138, v34
	v_mov_b32_e32 v139, v34
	v_mov_b32_e32 v140, v34
	v_mov_b32_e32 v141, v34
	v_mov_b32_e32 v142, v34
	v_mov_b32_e32 v143, v34
	v_mov_b32_e32 v144, v34
	v_mov_b32_e32 v145, v34
	v_mov_b32_e32 v146, v34
	v_mov_b32_e32 v147, v34
	v_mov_b32_e32 v148, v34
	v_mov_b32_e32 v149, v34
	v_mov_b32_e32 v150, v34
	v_mov_b32_e32 v151, v34
	v_mov_b32_e32 v152, v34
	v_mov_b32_e32 v153, v34
	v_mov_b32_e32 v158, v34
	v_mov_b32_e32 v159, v34
	v_mov_b32_e32 v160, v34
	v_mov_b32_e32 v161, v34
	v_mov_b32_e32 v154, v34
	v_mov_b32_e32 v155, v34
	v_mov_b32_e32 v156, v34
	v_mov_b32_e32 v157, v34
